# P1 EpiProj next-group L1 touch, waits relaxed to vmcnt(3) so the touches stay in flight; on top of v11
# baseline (speedup 1.0000x reference)
;     __device__ __forceinline__ void operator()(const f32x4 (&acc)[2][2][4][2], const Unit& u, int wr, int wc, int fr, int fq) const {
;     ...
;                 const int rit = ai * HALF + wr * 64 + m * 16 + fr, s = (u.pm & 15) * 256 + rit, grow = u.pm * 256 + rit;
;                 const float rs = rsqrtf(ss[grow] * (1.0f / 4096.0f) + RMS_EPS) * sc;
;                 f32x4 c0 = {1.f, 1.f, 1.f, 1.f}, c1 = c0, s0 = {0.f, 0.f, 0.f, 0.f}, s1 = s0;
;                 if (rope) { const float* t = cs + (size_t)s * 32 + 8 * (fq & 1); c0 = *(const f32x4*)t; c1 = *(const f32x4*)(t + 4); s0 = *(const f32x4*)(t + 16); s1 = *(const f32x4*)(t + 20); }
; #pragma unroll
;                 for (int bj = 0; bj < 2; ++bj) {
;                     f32x4 v0 = acc[ai][bj][m][0] * rs, v1 = acc[ai][bj][m][1] * rs;
;                     if (rope) { rope4(v0, c0, s0, fq); rope4(v1, c1, s1, fq); }
.LBB0_179:
	v_add_u32_e32 v246, s71, v187
	v_ashrrev_i32_e32 v247, 31, v246
	v_lshl_add_u64 v[246:247], v[246:247], 2, s[20:21]
	global_load_dword v248, v[246:247], off
	v_add_u32_e32 v246, s72, v187
	v_ashrrev_i32_e32 v247, 31, v246
	v_lshlrev_b64 v[246:247], 7, v[246:247]
	v_lshl_add_u64 v[246:247], v[156:157], 0, v[246:247]
	global_load_dword v249, v[246:247], off
	global_load_dword v249, v[246:247], off offset:64
	s_waitcnt vmcnt(3)
	v_fmamk_f32 v170, v170, 0x39800000, v197
	v_mul_f32_e32 v171, 0x4b800000, v170
	v_cmp_gt_f32_e32 vcc, s68, v170
	s_nop 1
	v_cndmask_b32_e32 v170, v170, v171, vcc
	v_rsq_f32_e32 v170, v170
	s_nop 0
	v_mul_f32_e32 v171, 0x45800000, v170
	v_cndmask_b32_e32 v176, v170, v171, vcc
	v_pk_mul_f32 v[170:171], v[124:125], v[176:177] op_sel_hi:[1,0]
	v_cndmask_b32_e64 v124, 0, 1, s[40:41]
	v_pk_mul_f32 v[178:179], v[128:129], v[176:177] op_sel_hi:[1,0]
	v_pk_mul_f32 v[182:183], v[126:127], v[176:177] op_sel_hi:[1,0]
	v_cmp_ne_u32_e64 s[12:13], 1, v124
	s_andn2_b64 vcc, exec, s[40:41]
	v_pk_mul_f32 v[174:175], v[122:123], v[176:177] op_sel_hi:[1,0]
	s_cbranch_vccnz .LBB0_186
	s_cmp_lt_i32 s43, 5
	s_cbranch_scc1 .LBB0_182
	s_cmp_lg_u32 s43, 5
	s_cselect_b64 s[10:11], -1, 0
	s_cbranch_execz .LBB0_183
	s_branch .LBB0_184

;     __device__ __forceinline__ void operator()(const f32x4 (&acc)[2][2][4][2], const Unit& u, int wr, int wc, int fr, int fq) const {
;     ...
;                 const int rit = ai * HALF + wr * 64 + m * 16 + fr, s = (u.pm & 15) * 256 + rit, grow = u.pm * 256 + rit;
;                 const float rs = rsqrtf(ss[grow] * (1.0f / 4096.0f) + RMS_EPS) * sc;
;                 f32x4 c0 = {1.f, 1.f, 1.f, 1.f}, c1 = c0, s0 = {0.f, 0.f, 0.f, 0.f}, s1 = s0;
;                 if (rope) { const float* t = cs + (size_t)s * 32 + 8 * (fq & 1); c0 = *(const f32x4*)t; c1 = *(const f32x4*)(t + 4); s0 = *(const f32x4*)(t + 16); s1 = *(const f32x4*)(t + 20); }
; #pragma unroll
;                 for (int bj = 0; bj < 2; ++bj) {
;                     f32x4 v0 = acc[ai][bj][m][0] * rs, v1 = acc[ai][bj][m][1] * rs;
.LBB0_217:
	v_add_u32_e32 v246, s71, v188
	v_ashrrev_i32_e32 v247, 31, v246
	v_lshl_add_u64 v[246:247], v[246:247], 2, s[20:21]
	global_load_dword v248, v[246:247], off
	v_add_u32_e32 v246, s72, v188
	v_ashrrev_i32_e32 v247, 31, v246
	v_lshlrev_b64 v[246:247], 7, v[246:247]
	v_lshl_add_u64 v[246:247], v[156:157], 0, v[246:247]
	global_load_dword v249, v[246:247], off
	global_load_dword v249, v[246:247], off offset:64
	s_waitcnt vmcnt(3)
	v_fmamk_f32 v130, v130, 0x39800000, v197
	v_mul_f32_e32 v131, 0x4b800000, v130
	v_cmp_gt_f32_e32 vcc, s68, v130
	s_nop 1
	v_cndmask_b32_e32 v130, v130, v131, vcc
	v_rsq_f32_e32 v130, v130
	s_nop 0
	v_mul_f32_e32 v131, 0x45800000, v130
	v_cndmask_b32_e32 v136, v130, v131, vcc
	v_pk_mul_f32 v[138:139], v[112:113], v[136:137] op_sel_hi:[1,0]
	v_pk_mul_f32 v[142:143], v[110:111], v[136:137] op_sel_hi:[1,0]
	v_pk_mul_f32 v[130:131], v[108:109], v[136:137] op_sel_hi:[1,0]
	s_and_b64 vcc, exec, s[12:13]
	v_pk_mul_f32 v[134:135], v[106:107], v[136:137] op_sel_hi:[1,0]
	s_cbranch_vccnz .LBB0_224
	s_cmp_lt_i32 s43, 5
	s_cbranch_scc1 .LBB0_220
	s_cmp_lg_u32 s43, 5
	s_cselect_b64 s[56:57], -1, 0
	s_cbranch_execz .LBB0_221
	s_branch .LBB0_222

;     __device__ __forceinline__ void operator()(const f32x4 (&acc)[2][2][4][2], const Unit& u, int wr, int wc, int fr, int fq) const {
;     ...
;                 const int rit = ai * HALF + wr * 64 + m * 16 + fr, s = (u.pm & 15) * 256 + rit, grow = u.pm * 256 + rit;
;                 const float rs = rsqrtf(ss[grow] * (1.0f / 4096.0f) + RMS_EPS) * sc;
;                 f32x4 c0 = {1.f, 1.f, 1.f, 1.f}, c1 = c0, s0 = {0.f, 0.f, 0.f, 0.f}, s1 = s0;
;                 if (rope) { const float* t = cs + (size_t)s * 32 + 8 * (fq & 1); c0 = *(const f32x4*)t; c1 = *(const f32x4*)(t + 4); s0 = *(const f32x4*)(t + 16); s1 = *(const f32x4*)(t + 20); }
; #pragma unroll
;                 for (int bj = 0; bj < 2; ++bj) {
;                     f32x4 v0 = acc[ai][bj][m][0] * rs, v1 = acc[ai][bj][m][1] * rs;
.LBB0_255:
	v_add_u32_e32 v246, s71, v189
	v_ashrrev_i32_e32 v247, 31, v246
	v_lshl_add_u64 v[246:247], v[246:247], 2, s[20:21]
	global_load_dword v248, v[246:247], off
	v_add_u32_e32 v246, s72, v189
	v_ashrrev_i32_e32 v247, 31, v246
	v_lshlrev_b64 v[246:247], 7, v[246:247]
	v_lshl_add_u64 v[246:247], v[156:157], 0, v[246:247]
	global_load_dword v249, v[246:247], off
	global_load_dword v249, v[246:247], off offset:64
	s_waitcnt vmcnt(3)
	v_fmamk_f32 v114, v114, 0x39800000, v197
	v_mul_f32_e32 v115, 0x4b800000, v114
	v_cmp_gt_f32_e32 vcc, s68, v114
	s_nop 1
	v_cndmask_b32_e32 v114, v114, v115, vcc
	v_rsq_f32_e32 v114, v114
	s_nop 0
	v_mul_f32_e32 v115, 0x45800000, v114
	v_cndmask_b32_e32 v120, v114, v115, vcc
	v_pk_mul_f32 v[122:123], v[96:97], v[120:121] op_sel_hi:[1,0]
	v_pk_mul_f32 v[126:127], v[94:95], v[120:121] op_sel_hi:[1,0]
	v_pk_mul_f32 v[114:115], v[92:93], v[120:121] op_sel_hi:[1,0]
	s_and_b64 vcc, exec, s[12:13]
	v_pk_mul_f32 v[118:119], v[90:91], v[120:121] op_sel_hi:[1,0]
	s_cbranch_vccnz .LBB0_262
	s_cmp_lt_i32 s43, 5
	s_cbranch_scc1 .LBB0_258
	s_cmp_lg_u32 s43, 5
	s_cselect_b64 s[56:57], -1, 0
	s_cbranch_execz .LBB0_259
	s_branch .LBB0_260

;     __device__ __forceinline__ void operator()(const f32x4 (&acc)[2][2][4][2], const Unit& u, int wr, int wc, int fr, int fq) const {
;     ...
;                 const int rit = ai * HALF + wr * 64 + m * 16 + fr, s = (u.pm & 15) * 256 + rit, grow = u.pm * 256 + rit;
;                 const float rs = rsqrtf(ss[grow] * (1.0f / 4096.0f) + RMS_EPS) * sc;
;                 f32x4 c0 = {1.f, 1.f, 1.f, 1.f}, c1 = c0, s0 = {0.f, 0.f, 0.f, 0.f}, s1 = s0;
;                 if (rope) { const float* t = cs + (size_t)s * 32 + 8 * (fq & 1); c0 = *(const f32x4*)t; c1 = *(const f32x4*)(t + 4); s0 = *(const f32x4*)(t + 16); s1 = *(const f32x4*)(t + 20); }
; #pragma unroll
;                 for (int bj = 0; bj < 2; ++bj) {
;                     f32x4 v0 = acc[ai][bj][m][0] * rs, v1 = acc[ai][bj][m][1] * rs;
.LBB0_293:
	v_add_u32_e32 v246, s71, v190
	v_ashrrev_i32_e32 v247, 31, v246
	v_lshl_add_u64 v[246:247], v[246:247], 2, s[20:21]
	global_load_dword v248, v[246:247], off
	v_add_u32_e32 v246, s72, v190
	v_ashrrev_i32_e32 v247, 31, v246
	v_lshlrev_b64 v[246:247], 7, v[246:247]
	v_lshl_add_u64 v[246:247], v[156:157], 0, v[246:247]
	global_load_dword v249, v[246:247], off
	global_load_dword v249, v[246:247], off offset:64
	s_waitcnt vmcnt(3)
	v_fmamk_f32 v98, v98, 0x39800000, v197
	v_mul_f32_e32 v99, 0x4b800000, v98
	v_cmp_gt_f32_e32 vcc, s68, v98
	s_nop 1
	v_cndmask_b32_e32 v98, v98, v99, vcc
	v_rsq_f32_e32 v98, v98
	s_nop 0
	v_mul_f32_e32 v99, 0x45800000, v98
	v_cndmask_b32_e32 v104, v98, v99, vcc
	v_pk_mul_f32 v[106:107], v[80:81], v[104:105] op_sel_hi:[1,0]
	v_pk_mul_f32 v[110:111], v[78:79], v[104:105] op_sel_hi:[1,0]
	v_pk_mul_f32 v[98:99], v[76:77], v[104:105] op_sel_hi:[1,0]
	s_and_b64 vcc, exec, s[12:13]
	v_pk_mul_f32 v[102:103], v[74:75], v[104:105] op_sel_hi:[1,0]
	s_cbranch_vccnz .LBB0_300
	s_cmp_lt_i32 s43, 5
	s_cbranch_scc1 .LBB0_296
	s_cmp_lg_u32 s43, 5
	s_cselect_b64 s[56:57], -1, 0
	s_cbranch_execz .LBB0_297
	s_branch .LBB0_298

;     __device__ __forceinline__ void operator()(const f32x4 (&acc)[2][2][4][2], const Unit& u, int wr, int wc, int fr, int fq) const {
;     ...
;                 const int rit = ai * HALF + wr * 64 + m * 16 + fr, s = (u.pm & 15) * 256 + rit, grow = u.pm * 256 + rit;
;                 const float rs = rsqrtf(ss[grow] * (1.0f / 4096.0f) + RMS_EPS) * sc;
;                 f32x4 c0 = {1.f, 1.f, 1.f, 1.f}, c1 = c0, s0 = {0.f, 0.f, 0.f, 0.f}, s1 = s0;
;                 if (rope) { const float* t = cs + (size_t)s * 32 + 8 * (fq & 1); c0 = *(const f32x4*)t; c1 = *(const f32x4*)(t + 4); s0 = *(const f32x4*)(t + 16); s1 = *(const f32x4*)(t + 20); }
; #pragma unroll
;                 for (int bj = 0; bj < 2; ++bj) {
;                     f32x4 v0 = acc[ai][bj][m][0] * rs, v1 = acc[ai][bj][m][1] * rs;
.LBB0_331:
	v_add_u32_e32 v246, s71, v191
	v_ashrrev_i32_e32 v247, 31, v246
	v_lshl_add_u64 v[246:247], v[246:247], 2, s[20:21]
	global_load_dword v248, v[246:247], off
	v_add_u32_e32 v246, s72, v191
	v_ashrrev_i32_e32 v247, 31, v246
	v_lshlrev_b64 v[246:247], 7, v[246:247]
	v_lshl_add_u64 v[246:247], v[156:157], 0, v[246:247]
	global_load_dword v249, v[246:247], off
	global_load_dword v249, v[246:247], off offset:64
	s_waitcnt vmcnt(3)
	v_fmamk_f32 v82, v82, 0x39800000, v197
	v_mul_f32_e32 v83, 0x4b800000, v82
	v_cmp_gt_f32_e32 vcc, s68, v82
	s_nop 1
	v_cndmask_b32_e32 v82, v82, v83, vcc
	v_rsq_f32_e32 v82, v82
	s_nop 0
	v_mul_f32_e32 v83, 0x45800000, v82
	v_cndmask_b32_e32 v88, v82, v83, vcc
	v_pk_mul_f32 v[90:91], v[64:65], v[88:89] op_sel_hi:[1,0]
	v_pk_mul_f32 v[94:95], v[62:63], v[88:89] op_sel_hi:[1,0]
	v_pk_mul_f32 v[82:83], v[60:61], v[88:89] op_sel_hi:[1,0]
	s_and_b64 vcc, exec, s[12:13]
	v_pk_mul_f32 v[86:87], v[58:59], v[88:89] op_sel_hi:[1,0]
	s_cbranch_vccnz .LBB0_338
	s_cmp_lt_i32 s43, 5
	s_cbranch_scc1 .LBB0_334
	s_cmp_lg_u32 s43, 5
	s_cselect_b64 s[56:57], -1, 0
	s_cbranch_execz .LBB0_335
	s_branch .LBB0_336

;     __device__ __forceinline__ void operator()(const f32x4 (&acc)[2][2][4][2], const Unit& u, int wr, int wc, int fr, int fq) const {
;     ...
;                 const int rit = ai * HALF + wr * 64 + m * 16 + fr, s = (u.pm & 15) * 256 + rit, grow = u.pm * 256 + rit;
;                 const float rs = rsqrtf(ss[grow] * (1.0f / 4096.0f) + RMS_EPS) * sc;
;                 f32x4 c0 = {1.f, 1.f, 1.f, 1.f}, c1 = c0, s0 = {0.f, 0.f, 0.f, 0.f}, s1 = s0;
;                 if (rope) { const float* t = cs + (size_t)s * 32 + 8 * (fq & 1); c0 = *(const f32x4*)t; c1 = *(const f32x4*)(t + 4); s0 = *(const f32x4*)(t + 16); s1 = *(const f32x4*)(t + 20); }
; #pragma unroll
;                 for (int bj = 0; bj < 2; ++bj) {
;                     f32x4 v0 = acc[ai][bj][m][0] * rs, v1 = acc[ai][bj][m][1] * rs;
.LBB0_369:
	v_add_u32_e32 v246, s71, v192
	v_ashrrev_i32_e32 v247, 31, v246
	v_lshl_add_u64 v[246:247], v[246:247], 2, s[20:21]
	global_load_dword v248, v[246:247], off
	v_add_u32_e32 v246, s72, v192
	v_ashrrev_i32_e32 v247, 31, v246
	v_lshlrev_b64 v[246:247], 7, v[246:247]
	v_lshl_add_u64 v[246:247], v[156:157], 0, v[246:247]
	global_load_dword v249, v[246:247], off
	global_load_dword v249, v[246:247], off offset:64
	s_waitcnt vmcnt(3)
	v_fmamk_f32 v66, v66, 0x39800000, v197
	v_mul_f32_e32 v67, 0x4b800000, v66
	v_cmp_gt_f32_e32 vcc, s68, v66
	s_nop 1
	v_cndmask_b32_e32 v66, v66, v67, vcc
	v_rsq_f32_e32 v66, v66
	s_nop 0
	v_mul_f32_e32 v67, 0x45800000, v66
	v_cndmask_b32_e32 v72, v66, v67, vcc
	v_pk_mul_f32 v[74:75], v[48:49], v[72:73] op_sel_hi:[1,0]
	v_pk_mul_f32 v[78:79], v[46:47], v[72:73] op_sel_hi:[1,0]
	v_pk_mul_f32 v[66:67], v[44:45], v[72:73] op_sel_hi:[1,0]
	s_and_b64 vcc, exec, s[12:13]
	v_pk_mul_f32 v[70:71], v[42:43], v[72:73] op_sel_hi:[1,0]
	s_cbranch_vccnz .LBB0_376
	s_cmp_lt_i32 s43, 5
	s_cbranch_scc1 .LBB0_372
	s_cmp_lg_u32 s43, 5
	s_cselect_b64 s[56:57], -1, 0
	s_cbranch_execz .LBB0_373
	s_branch .LBB0_374

;     __device__ __forceinline__ void operator()(const f32x4 (&acc)[2][2][4][2], const Unit& u, int wr, int wc, int fr, int fq) const {
;     ...
;                 const int rit = ai * HALF + wr * 64 + m * 16 + fr, s = (u.pm & 15) * 256 + rit, grow = u.pm * 256 + rit;
;                 const float rs = rsqrtf(ss[grow] * (1.0f / 4096.0f) + RMS_EPS) * sc;
;                 f32x4 c0 = {1.f, 1.f, 1.f, 1.f}, c1 = c0, s0 = {0.f, 0.f, 0.f, 0.f}, s1 = s0;
;                 if (rope) { const float* t = cs + (size_t)s * 32 + 8 * (fq & 1); c0 = *(const f32x4*)t; c1 = *(const f32x4*)(t + 4); s0 = *(const f32x4*)(t + 16); s1 = *(const f32x4*)(t + 20); }
; #pragma unroll
;                 for (int bj = 0; bj < 2; ++bj) {
;                     f32x4 v0 = acc[ai][bj][m][0] * rs, v1 = acc[ai][bj][m][1] * rs;
.LBB0_407:
	v_add_u32_e32 v246, s71, v193
	v_ashrrev_i32_e32 v247, 31, v246
	v_lshl_add_u64 v[246:247], v[246:247], 2, s[20:21]
	global_load_dword v248, v[246:247], off
	v_add_u32_e32 v246, s72, v193
	v_ashrrev_i32_e32 v247, 31, v246
	v_lshlrev_b64 v[246:247], 7, v[246:247]
	v_lshl_add_u64 v[246:247], v[156:157], 0, v[246:247]
	global_load_dword v249, v[246:247], off
	global_load_dword v249, v[246:247], off offset:64
	s_waitcnt vmcnt(3)
	v_fmamk_f32 v50, v50, 0x39800000, v197
	v_mul_f32_e32 v51, 0x4b800000, v50
	v_cmp_gt_f32_e32 vcc, s68, v50
	s_nop 1
	v_cndmask_b32_e32 v50, v50, v51, vcc
	v_rsq_f32_e32 v50, v50
	s_nop 0
	v_mul_f32_e32 v51, 0x45800000, v50
	v_cndmask_b32_e32 v56, v50, v51, vcc
	v_pk_mul_f32 v[58:59], v[32:33], v[56:57] op_sel_hi:[1,0]
	v_pk_mul_f32 v[62:63], v[30:31], v[56:57] op_sel_hi:[1,0]
	v_pk_mul_f32 v[50:51], v[28:29], v[56:57] op_sel_hi:[1,0]
	s_and_b64 vcc, exec, s[12:13]
	v_pk_mul_f32 v[54:55], v[26:27], v[56:57] op_sel_hi:[1,0]
	s_cbranch_vccnz .LBB0_414
	s_cmp_lt_i32 s43, 5
	s_cbranch_scc1 .LBB0_410
	s_cmp_lg_u32 s43, 5
	s_cselect_b64 s[56:57], -1, 0
	s_cbranch_execz .LBB0_411
	s_branch .LBB0_412

;     __device__ __forceinline__ void operator()(const f32x4 (&acc)[2][2][4][2], const Unit& u, int wr, int wc, int fr, int fq) const {
;     ...
;                 const int rit = ai * HALF + wr * 64 + m * 16 + fr, s = (u.pm & 15) * 256 + rit, grow = u.pm * 256 + rit;
;                 const float rs = rsqrtf(ss[grow] * (1.0f / 4096.0f) + RMS_EPS) * sc;
;                 f32x4 c0 = {1.f, 1.f, 1.f, 1.f}, c1 = c0, s0 = {0.f, 0.f, 0.f, 0.f}, s1 = s0;
;                 if (rope) { const float* t = cs + (size_t)s * 32 + 8 * (fq & 1); c0 = *(const f32x4*)t; c1 = *(const f32x4*)(t + 4); s0 = *(const f32x4*)(t + 16); s1 = *(const f32x4*)(t + 20); }
; #pragma unroll
;                 for (int bj = 0; bj < 2; ++bj) {
;                     f32x4 v0 = acc[ai][bj][m][0] * rs, v1 = acc[ai][bj][m][1] * rs;
.LBB0_545:
	v_add_u32_e32 v246, s69, v195
	v_ashrrev_i32_e32 v247, 31, v246
	v_lshl_add_u64 v[246:247], v[246:247], 2, s[20:21]
	global_load_dword v248, v[246:247], off
	v_add_u32_e32 v246, s70, v195
	v_ashrrev_i32_e32 v247, 31, v246
	v_lshlrev_b64 v[246:247], 7, v[246:247]
	v_lshl_add_u64 v[246:247], v[172:173], 0, v[246:247]
	global_load_dword v249, v[246:247], off
	global_load_dword v249, v[246:247], off offset:64
	s_waitcnt vmcnt(3)
	v_fmamk_f32 v18, v18, 0x39800000, v205
	v_mul_f32_e32 v19, 0x4b800000, v18
	v_cmp_gt_f32_e32 vcc, s66, v18
	v_cndmask_b32_e64 v21, 0, 1, s[38:39]
	v_cmp_ne_u32_e64 s[10:11], 1, v21
	v_cndmask_b32_e32 v18, v18, v19, vcc
	v_rsq_f32_e32 v18, v18
	s_nop 0
	v_mul_f32_e32 v19, 0x45800000, v18
	v_cndmask_b32_e32 v18, v18, v19, vcc
	v_mul_f32_e32 v24, 0x3c800000, v18
	v_pk_mul_f32 v[26:27], v[160:161], v[24:25] op_sel_hi:[1,0]
	v_pk_mul_f32 v[30:31], v[158:159], v[24:25] op_sel_hi:[1,0]
	v_pk_mul_f32 v[18:19], v[156:157], v[24:25] op_sel_hi:[1,0]
	s_andn2_b64 vcc, exec, s[38:39]
	v_pk_mul_f32 v[22:23], v[154:155], v[24:25] op_sel_hi:[1,0]
	s_cbranch_vccnz .LBB0_552
	s_cmp_lt_i32 s3, 2
	s_cbranch_scc1 .LBB0_548
	s_cmp_lg_u32 s3, 2
	s_cselect_b64 s[8:9], -1, 0
	s_cbranch_execz .LBB0_549
	s_branch .LBB0_550

;     __device__ __forceinline__ void operator()(const f32x4 (&acc)[2][2][4][2], const Unit& u, int wr, int wc, int fr, int fq) const {
;     ...
;                 const int rit = ai * HALF + wr * 64 + m * 16 + fr, s = (u.pm & 15) * 256 + rit, grow = u.pm * 256 + rit;
;                 const float rs = rsqrtf(ss[grow] * (1.0f / 4096.0f) + RMS_EPS) * sc;
;                 f32x4 c0 = {1.f, 1.f, 1.f, 1.f}, c1 = c0, s0 = {0.f, 0.f, 0.f, 0.f}, s1 = s0;
;                 if (rope) { const float* t = cs + (size_t)s * 32 + 8 * (fq & 1); c0 = *(const f32x4*)t; c1 = *(const f32x4*)(t + 4); s0 = *(const f32x4*)(t + 16); s1 = *(const f32x4*)(t + 20); }
; #pragma unroll
;                 for (int bj = 0; bj < 2; ++bj) {
;                     f32x4 v0 = acc[ai][bj][m][0] * rs, v1 = acc[ai][bj][m][1] * rs;
.LBB0_583:
	v_add_u32_e32 v246, s69, v196
	v_ashrrev_i32_e32 v247, 31, v246
	v_lshl_add_u64 v[246:247], v[246:247], 2, s[20:21]
	global_load_dword v248, v[246:247], off
	v_add_u32_e32 v246, s70, v196
	v_ashrrev_i32_e32 v247, 31, v246
	v_lshlrev_b64 v[246:247], 7, v[246:247]
	v_lshl_add_u64 v[246:247], v[172:173], 0, v[246:247]
	global_load_dword v249, v[246:247], off
	global_load_dword v249, v[246:247], off offset:64
	s_waitcnt vmcnt(3)
	v_fmamk_f32 v147, v148, 0x39800000, v205
	v_mul_f32_e32 v148, 0x4b800000, v147
	v_cmp_gt_f32_e32 vcc, s66, v147
	s_nop 1
	v_cndmask_b32_e32 v147, v147, v148, vcc
	v_rsq_f32_e32 v147, v147
	s_nop 0
	v_mul_f32_e32 v148, 0x45800000, v147
	v_cndmask_b32_e32 v147, v147, v148, vcc
	v_mul_f32_e32 v148, 0x3c800000, v147
	v_pk_mul_f32 v[144:145], v[144:145], v[148:149] op_sel_hi:[1,0]
	v_pk_mul_f32 v[142:143], v[142:143], v[148:149] op_sel_hi:[1,0]
	v_pk_mul_f32 v[140:141], v[140:141], v[148:149] op_sel_hi:[1,0]
	s_and_b64 vcc, exec, s[10:11]
	v_pk_mul_f32 v[138:139], v[138:139], v[148:149] op_sel_hi:[1,0]
	s_cbranch_vccnz .LBB0_590
	s_cmp_lt_i32 s3, 2
	s_cbranch_scc1 .LBB0_586
	s_cmp_lg_u32 s3, 2
	s_cselect_b64 s[52:53], -1, 0
	s_cbranch_execz .LBB0_587
	s_branch .LBB0_588

;     __device__ __forceinline__ void operator()(const f32x4 (&acc)[2][2][4][2], const Unit& u, int wr, int wc, int fr, int fq) const {
;     ...
;                 const int rit = ai * HALF + wr * 64 + m * 16 + fr, s = (u.pm & 15) * 256 + rit, grow = u.pm * 256 + rit;
;                 const float rs = rsqrtf(ss[grow] * (1.0f / 4096.0f) + RMS_EPS) * sc;
;                 f32x4 c0 = {1.f, 1.f, 1.f, 1.f}, c1 = c0, s0 = {0.f, 0.f, 0.f, 0.f}, s1 = s0;
;                 if (rope) { const float* t = cs + (size_t)s * 32 + 8 * (fq & 1); c0 = *(const f32x4*)t; c1 = *(const f32x4*)(t + 4); s0 = *(const f32x4*)(t + 16); s1 = *(const f32x4*)(t + 20); }
; #pragma unroll
;                 for (int bj = 0; bj < 2; ++bj) {
;                     f32x4 v0 = acc[ai][bj][m][0] * rs, v1 = acc[ai][bj][m][1] * rs;
.LBB0_621:
	v_add_u32_e32 v246, s69, v197
	v_ashrrev_i32_e32 v247, 31, v246
	v_lshl_add_u64 v[246:247], v[246:247], 2, s[20:21]
	global_load_dword v248, v[246:247], off
	v_add_u32_e32 v246, s70, v197
	v_ashrrev_i32_e32 v247, 31, v246
	v_lshlrev_b64 v[246:247], 7, v[246:247]
	v_lshl_add_u64 v[246:247], v[172:173], 0, v[246:247]
	global_load_dword v249, v[246:247], off
	global_load_dword v249, v[246:247], off offset:64
	s_waitcnt vmcnt(3)
	v_fmamk_f32 v147, v148, 0x39800000, v205
	v_mul_f32_e32 v148, 0x4b800000, v147
	v_cmp_gt_f32_e32 vcc, s66, v147
	s_nop 1
	v_cndmask_b32_e32 v147, v147, v148, vcc
	v_rsq_f32_e32 v147, v147
	s_nop 0
	v_mul_f32_e32 v148, 0x45800000, v147
	v_cndmask_b32_e32 v147, v147, v148, vcc
	v_mul_f32_e32 v148, 0x3c800000, v147
	v_pk_mul_f32 v[128:129], v[128:129], v[148:149] op_sel_hi:[1,0]
	v_pk_mul_f32 v[126:127], v[126:127], v[148:149] op_sel_hi:[1,0]
	v_pk_mul_f32 v[124:125], v[124:125], v[148:149] op_sel_hi:[1,0]
	s_and_b64 vcc, exec, s[10:11]
	v_pk_mul_f32 v[122:123], v[122:123], v[148:149] op_sel_hi:[1,0]
	s_cbranch_vccnz .LBB0_628
	s_cmp_lt_i32 s3, 2
	s_cbranch_scc1 .LBB0_624
	s_cmp_lg_u32 s3, 2
	s_cselect_b64 s[52:53], -1, 0
	s_cbranch_execz .LBB0_625
	s_branch .LBB0_626

;     __device__ __forceinline__ void operator()(const f32x4 (&acc)[2][2][4][2], const Unit& u, int wr, int wc, int fr, int fq) const {
;     ...
;                 const int rit = ai * HALF + wr * 64 + m * 16 + fr, s = (u.pm & 15) * 256 + rit, grow = u.pm * 256 + rit;
;                 const float rs = rsqrtf(ss[grow] * (1.0f / 4096.0f) + RMS_EPS) * sc;
;                 f32x4 c0 = {1.f, 1.f, 1.f, 1.f}, c1 = c0, s0 = {0.f, 0.f, 0.f, 0.f}, s1 = s0;
;                 if (rope) { const float* t = cs + (size_t)s * 32 + 8 * (fq & 1); c0 = *(const f32x4*)t; c1 = *(const f32x4*)(t + 4); s0 = *(const f32x4*)(t + 16); s1 = *(const f32x4*)(t + 20); }
; #pragma unroll
;                 for (int bj = 0; bj < 2; ++bj) {
;                     f32x4 v0 = acc[ai][bj][m][0] * rs, v1 = acc[ai][bj][m][1] * rs;
.LBB0_659:
	v_add_u32_e32 v246, s69, v198
	v_ashrrev_i32_e32 v247, 31, v246
	v_lshl_add_u64 v[246:247], v[246:247], 2, s[20:21]
	global_load_dword v248, v[246:247], off
	v_add_u32_e32 v246, s70, v198
	v_ashrrev_i32_e32 v247, 31, v246
	v_lshlrev_b64 v[246:247], 7, v[246:247]
	v_lshl_add_u64 v[246:247], v[172:173], 0, v[246:247]
	global_load_dword v249, v[246:247], off
	global_load_dword v249, v[246:247], off offset:64
	s_waitcnt vmcnt(3)
	v_fmamk_f32 v147, v148, 0x39800000, v205
	v_mul_f32_e32 v148, 0x4b800000, v147
	v_cmp_gt_f32_e32 vcc, s66, v147
	s_nop 1
	v_cndmask_b32_e32 v147, v147, v148, vcc
	v_rsq_f32_e32 v147, v147
	s_nop 0
	v_mul_f32_e32 v148, 0x45800000, v147
	v_cndmask_b32_e32 v147, v147, v148, vcc
	v_mul_f32_e32 v148, 0x3c800000, v147
	v_pk_mul_f32 v[112:113], v[112:113], v[148:149] op_sel_hi:[1,0]
	v_pk_mul_f32 v[110:111], v[110:111], v[148:149] op_sel_hi:[1,0]
	v_pk_mul_f32 v[108:109], v[108:109], v[148:149] op_sel_hi:[1,0]
	s_and_b64 vcc, exec, s[10:11]
	v_pk_mul_f32 v[106:107], v[106:107], v[148:149] op_sel_hi:[1,0]
	s_cbranch_vccnz .LBB0_666
	s_cmp_lt_i32 s3, 2
	s_cbranch_scc1 .LBB0_662
	s_cmp_lg_u32 s3, 2
	s_cselect_b64 s[52:53], -1, 0
	s_cbranch_execz .LBB0_663
	s_branch .LBB0_664

;     __device__ __forceinline__ void operator()(const f32x4 (&acc)[2][2][4][2], const Unit& u, int wr, int wc, int fr, int fq) const {
;     ...
;                 const int rit = ai * HALF + wr * 64 + m * 16 + fr, s = (u.pm & 15) * 256 + rit, grow = u.pm * 256 + rit;
;                 const float rs = rsqrtf(ss[grow] * (1.0f / 4096.0f) + RMS_EPS) * sc;
;                 f32x4 c0 = {1.f, 1.f, 1.f, 1.f}, c1 = c0, s0 = {0.f, 0.f, 0.f, 0.f}, s1 = s0;
;                 if (rope) { const float* t = cs + (size_t)s * 32 + 8 * (fq & 1); c0 = *(const f32x4*)t; c1 = *(const f32x4*)(t + 4); s0 = *(const f32x4*)(t + 16); s1 = *(const f32x4*)(t + 20); }
; #pragma unroll
;                 for (int bj = 0; bj < 2; ++bj) {
;                     f32x4 v0 = acc[ai][bj][m][0] * rs, v1 = acc[ai][bj][m][1] * rs;
.LBB0_697:
	v_add_u32_e32 v246, s69, v199
	v_ashrrev_i32_e32 v247, 31, v246
	v_lshl_add_u64 v[246:247], v[246:247], 2, s[20:21]
	global_load_dword v248, v[246:247], off
	v_add_u32_e32 v246, s70, v199
	v_ashrrev_i32_e32 v247, 31, v246
	v_lshlrev_b64 v[246:247], 7, v[246:247]
	v_lshl_add_u64 v[246:247], v[172:173], 0, v[246:247]
	global_load_dword v249, v[246:247], off
	global_load_dword v249, v[246:247], off offset:64
	s_waitcnt vmcnt(3)
	v_fmamk_f32 v147, v148, 0x39800000, v205
	v_mul_f32_e32 v148, 0x4b800000, v147
	v_cmp_gt_f32_e32 vcc, s66, v147
	s_nop 1
	v_cndmask_b32_e32 v147, v147, v148, vcc
	v_rsq_f32_e32 v147, v147
	s_nop 0
	v_mul_f32_e32 v148, 0x45800000, v147
	v_cndmask_b32_e32 v147, v147, v148, vcc
	v_mul_f32_e32 v148, 0x3c800000, v147
	v_pk_mul_f32 v[96:97], v[96:97], v[148:149] op_sel_hi:[1,0]
	v_pk_mul_f32 v[94:95], v[94:95], v[148:149] op_sel_hi:[1,0]
	v_pk_mul_f32 v[92:93], v[92:93], v[148:149] op_sel_hi:[1,0]
	s_and_b64 vcc, exec, s[10:11]
	v_pk_mul_f32 v[90:91], v[90:91], v[148:149] op_sel_hi:[1,0]
	s_cbranch_vccnz .LBB0_704
	s_cmp_lt_i32 s3, 2
	s_cbranch_scc1 .LBB0_700
	s_cmp_lg_u32 s3, 2
	s_cselect_b64 s[52:53], -1, 0
	s_cbranch_execz .LBB0_701
	s_branch .LBB0_702

;     __device__ __forceinline__ void operator()(const f32x4 (&acc)[2][2][4][2], const Unit& u, int wr, int wc, int fr, int fq) const {
;     ...
;                 const int rit = ai * HALF + wr * 64 + m * 16 + fr, s = (u.pm & 15) * 256 + rit, grow = u.pm * 256 + rit;
;                 const float rs = rsqrtf(ss[grow] * (1.0f / 4096.0f) + RMS_EPS) * sc;
;                 f32x4 c0 = {1.f, 1.f, 1.f, 1.f}, c1 = c0, s0 = {0.f, 0.f, 0.f, 0.f}, s1 = s0;
;                 if (rope) { const float* t = cs + (size_t)s * 32 + 8 * (fq & 1); c0 = *(const f32x4*)t; c1 = *(const f32x4*)(t + 4); s0 = *(const f32x4*)(t + 16); s1 = *(const f32x4*)(t + 20); }
; #pragma unroll
;                 for (int bj = 0; bj < 2; ++bj) {
;                     f32x4 v0 = acc[ai][bj][m][0] * rs, v1 = acc[ai][bj][m][1] * rs;
.LBB0_735:
	v_add_u32_e32 v246, s69, v200
	v_ashrrev_i32_e32 v247, 31, v246
	v_lshl_add_u64 v[246:247], v[246:247], 2, s[20:21]
	global_load_dword v248, v[246:247], off
	v_add_u32_e32 v246, s70, v200
	v_ashrrev_i32_e32 v247, 31, v246
	v_lshlrev_b64 v[246:247], 7, v[246:247]
	v_lshl_add_u64 v[246:247], v[172:173], 0, v[246:247]
	global_load_dword v249, v[246:247], off
	global_load_dword v249, v[246:247], off offset:64
	s_waitcnt vmcnt(3)
	v_fmamk_f32 v147, v148, 0x39800000, v205
	v_mul_f32_e32 v148, 0x4b800000, v147
	v_cmp_gt_f32_e32 vcc, s66, v147
	s_nop 1
	v_cndmask_b32_e32 v147, v147, v148, vcc
	v_rsq_f32_e32 v147, v147
	s_nop 0
	v_mul_f32_e32 v148, 0x45800000, v147
	v_cndmask_b32_e32 v147, v147, v148, vcc
	v_mul_f32_e32 v148, 0x3c800000, v147
	v_pk_mul_f32 v[80:81], v[80:81], v[148:149] op_sel_hi:[1,0]
	v_pk_mul_f32 v[78:79], v[78:79], v[148:149] op_sel_hi:[1,0]
	v_pk_mul_f32 v[76:77], v[76:77], v[148:149] op_sel_hi:[1,0]
	s_and_b64 vcc, exec, s[10:11]
	v_pk_mul_f32 v[74:75], v[74:75], v[148:149] op_sel_hi:[1,0]
	s_cbranch_vccnz .LBB0_742
	s_cmp_lt_i32 s3, 2
	s_cbranch_scc1 .LBB0_738
	s_cmp_lg_u32 s3, 2
	s_cselect_b64 s[52:53], -1, 0
	s_cbranch_execz .LBB0_739
	s_branch .LBB0_740

;     __device__ __forceinline__ void operator()(const f32x4 (&acc)[2][2][4][2], const Unit& u, int wr, int wc, int fr, int fq) const {
;     ...
;                 const int rit = ai * HALF + wr * 64 + m * 16 + fr, s = (u.pm & 15) * 256 + rit, grow = u.pm * 256 + rit;
;                 const float rs = rsqrtf(ss[grow] * (1.0f / 4096.0f) + RMS_EPS) * sc;
;                 f32x4 c0 = {1.f, 1.f, 1.f, 1.f}, c1 = c0, s0 = {0.f, 0.f, 0.f, 0.f}, s1 = s0;
;                 if (rope) { const float* t = cs + (size_t)s * 32 + 8 * (fq & 1); c0 = *(const f32x4*)t; c1 = *(const f32x4*)(t + 4); s0 = *(const f32x4*)(t + 16); s1 = *(const f32x4*)(t + 20); }
; #pragma unroll
;                 for (int bj = 0; bj < 2; ++bj) {
;                     f32x4 v0 = acc[ai][bj][m][0] * rs, v1 = acc[ai][bj][m][1] * rs;
.LBB0_773:
	v_add_u32_e32 v246, s69, v201
	v_ashrrev_i32_e32 v247, 31, v246
	v_lshl_add_u64 v[246:247], v[246:247], 2, s[20:21]
	global_load_dword v248, v[246:247], off
	v_add_u32_e32 v246, s70, v201
	v_ashrrev_i32_e32 v247, 31, v246
	v_lshlrev_b64 v[246:247], 7, v[246:247]
	v_lshl_add_u64 v[246:247], v[172:173], 0, v[246:247]
	global_load_dword v249, v[246:247], off
	global_load_dword v249, v[246:247], off offset:64
	s_waitcnt vmcnt(3)
	v_fmamk_f32 v147, v148, 0x39800000, v205
	v_mul_f32_e32 v148, 0x4b800000, v147
	v_cmp_gt_f32_e32 vcc, s66, v147
	s_nop 1
	v_cndmask_b32_e32 v147, v147, v148, vcc
	v_rsq_f32_e32 v147, v147
	s_nop 0
	v_mul_f32_e32 v148, 0x45800000, v147
	v_cndmask_b32_e32 v147, v147, v148, vcc
	v_mul_f32_e32 v148, 0x3c800000, v147
	v_pk_mul_f32 v[64:65], v[64:65], v[148:149] op_sel_hi:[1,0]
	v_pk_mul_f32 v[62:63], v[62:63], v[148:149] op_sel_hi:[1,0]
	v_pk_mul_f32 v[60:61], v[60:61], v[148:149] op_sel_hi:[1,0]
	s_and_b64 vcc, exec, s[10:11]
	v_pk_mul_f32 v[58:59], v[58:59], v[148:149] op_sel_hi:[1,0]
	s_cbranch_vccnz .LBB0_780
	s_cmp_lt_i32 s3, 2
	s_cbranch_scc1 .LBB0_776
	s_cmp_lg_u32 s3, 2
	s_cselect_b64 s[52:53], -1, 0
	s_cbranch_execz .LBB0_777
	s_branch .LBB0_778
